# attention S stage: K fragment reads for all 10 key tiles issued ahead of the MFMAs
# baseline (speedup 1.0000x reference)
.LBB0_559:
	v_lshl_add_u64 v[2:3], v[60:61], 0, s[10:11]
	v_add_co_u32_e32 v6, vcc, 0x3bc4a000, v2
	v_min_u32_e32 v88, 6, v42
	s_nop 0
	v_addc_co_u32_e32 v7, vcc, 0, v3, vcc
	global_load_dwordx4 v[2:5], v[6:7], off
	global_load_dwordx4 v[90:93], v[6:7], off offset:64
	v_lshlrev_b32_e32 v89, 4, v88
	v_add_u32_e32 v98, 16, v89
	v_add_u32_e32 v87, 2, v88
	v_lshlrev_b32_e32 v99, 4, v87
	v_add_u32_e32 v100, 48, v89
	v_add_u32_e32 v86, 4, v88
	v_lshlrev_b32_e32 v101, 4, v86
	v_add_u32_e32 v102, 0x50, v89
	v_add_u32_e32 v59, 6, v88
	v_lshlrev_b32_e32 v103, 4, v59
	v_add_u32_e32 v104, 0x70, v89
	v_or_b32_e32 v57, 8, v88
	v_lshlrev_b32_e32 v105, 4, v57
	v_add_u32_e32 v106, 0x90, v89
	v_or_b32_e32 v200, v89, v1
	v_mad_u32_u24 v201, v200, s17, v65
	ds_read_b128 v[120:123], v201
	ds_read_b128 v[124:127], v201 offset:64
	v_or_b32_e32 v200, v98, v1
	v_mad_u32_u24 v201, v200, s17, v65
	ds_read_b128 v[128:131], v201
	ds_read_b128 v[132:135], v201 offset:64
	v_or_b32_e32 v200, v99, v1
	v_mad_u32_u24 v201, v200, s17, v65
	ds_read_b128 v[136:139], v201
	ds_read_b128 v[140:143], v201 offset:64
	v_or_b32_e32 v200, v100, v1
	v_mad_u32_u24 v201, v200, s17, v65
	ds_read_b128 v[144:147], v201
	ds_read_b128 v[148:151], v201 offset:64
	v_or_b32_e32 v200, v101, v1
	v_mad_u32_u24 v201, v200, s17, v65
	ds_read_b128 v[152:155], v201
	ds_read_b128 v[156:159], v201 offset:64
	v_or_b32_e32 v200, v102, v1
	v_mad_u32_u24 v201, v200, s17, v65
	ds_read_b128 v[160:163], v201
	ds_read_b128 v[164:167], v201 offset:64
	v_or_b32_e32 v200, v103, v1
	v_mad_u32_u24 v201, v200, s17, v65
	ds_read_b128 v[168:171], v201
	ds_read_b128 v[172:175], v201 offset:64
	v_or_b32_e32 v200, v104, v1
	v_mad_u32_u24 v201, v200, s17, v65
	ds_read_b128 v[176:179], v201
	ds_read_b128 v[180:183], v201 offset:64
	v_or_b32_e32 v200, v105, v1
	v_mad_u32_u24 v201, v200, s17, v65
	ds_read_b128 v[184:187], v201
	ds_read_b128 v[188:191], v201 offset:64
	v_or_b32_e32 v200, v106, v1
	v_mad_u32_u24 v201, v200, s17, v65
	ds_read_b128 v[192:195], v201
	ds_read_b128 v[196:199], v201 offset:64
	v_or_b32_e32 v89, v89, v66
	v_cmp_gt_u32_e32 vcc, v89, v55
	v_cmp_lt_i32_e64 s[4:5], s8, v89
	s_and_b64 vcc, vcc, s[4:5]
	v_cmp_le_i32_e64 s[4:5], s8, v89
	v_add_u32_e32 v42, 1, v42
	s_waitcnt vmcnt(0)
	s_waitcnt lgkmcnt(15)
	v_mfma_f32_16x16x32_bf16 v[38:41], v[120:123], v[2:5], 0
	v_mfma_f32_16x16x32_bf16 v[38:41], v[124:127], v[90:93], v[38:41]
	s_waitcnt lgkmcnt(15)
	v_mfma_f32_16x16x32_bf16 v[34:37], v[128:131], v[2:5], 0
	v_mfma_f32_16x16x32_bf16 v[34:37], v[132:135], v[90:93], v[34:37]
	s_waitcnt lgkmcnt(14)
	v_mfma_f32_16x16x32_bf16 v[30:33], v[136:139], v[2:5], 0
	v_mfma_f32_16x16x32_bf16 v[30:33], v[140:143], v[90:93], v[30:33]
	s_waitcnt lgkmcnt(12)
	v_mfma_f32_16x16x32_bf16 v[26:29], v[144:147], v[2:5], 0
	v_mfma_f32_16x16x32_bf16 v[26:29], v[148:151], v[90:93], v[26:29]
	s_waitcnt lgkmcnt(10)
	v_mfma_f32_16x16x32_bf16 v[22:25], v[152:155], v[2:5], 0
	v_mfma_f32_16x16x32_bf16 v[22:25], v[156:159], v[90:93], v[22:25]
	s_waitcnt lgkmcnt(8)
	v_mfma_f32_16x16x32_bf16 v[18:21], v[160:163], v[2:5], 0
	v_mfma_f32_16x16x32_bf16 v[18:21], v[164:167], v[90:93], v[18:21]
	s_waitcnt lgkmcnt(6)
	v_mfma_f32_16x16x32_bf16 v[14:17], v[168:171], v[2:5], 0
	v_mfma_f32_16x16x32_bf16 v[14:17], v[172:175], v[90:93], v[14:17]
	s_waitcnt lgkmcnt(4)
	v_mfma_f32_16x16x32_bf16 v[10:13], v[176:179], v[2:5], 0
	v_mfma_f32_16x16x32_bf16 v[10:13], v[180:183], v[90:93], v[10:13]
	s_waitcnt lgkmcnt(2)
	v_mfma_f32_16x16x32_bf16 v[6:9], v[184:187], v[2:5], 0
	v_mfma_f32_16x16x32_bf16 v[6:9], v[188:191], v[90:93], v[6:9]
	s_waitcnt lgkmcnt(0)
	v_mfma_f32_16x16x32_bf16 v[2:5], v[192:195], v[2:5], 0
	v_mfma_f32_16x16x32_bf16 v[2:5], v[196:199], v[90:93], v[2:5]
	s_nop 7
	s_nop 1
	v_cndmask_b32_e32 v38, v85, v38, vcc
	v_cmp_ge_u32_e32 vcc, v89, v55
	s_and_b64 vcc, vcc, s[4:5]
	s_nop 1
	v_cndmask_b32_e32 v39, v85, v39, vcc
	v_or_b32_e32 v92, 2, v89
	v_cmp_gt_u32_e32 vcc, v92, v55
	v_cmp_lt_i32_e64 s[4:5], s8, v92
	s_and_b64 vcc, vcc, s[4:5]
	v_or_b32_e32 v89, 3, v89
	v_cndmask_b32_e32 v40, v85, v40, vcc
	v_cmp_gt_u32_e32 vcc, v89, v55
	v_cmp_lt_i32_e64 s[4:5], s8, v89
	s_and_b64 vcc, vcc, s[4:5]
	v_max3_f32 v91, v38, s20, v39
	v_cndmask_b32_e32 v41, v85, v41, vcc
	v_max3_f32 v89, v91, v40, v41
	v_or_b32_e32 v91, v98, v66
	v_cmp_gt_u32_e32 vcc, v91, v55
	v_cmp_lt_i32_e64 s[4:5], s8, v91
	s_and_b64 vcc, vcc, s[4:5]
	v_cndmask_b32_e32 v34, v85, v34, vcc
	v_cmp_ge_u32_e32 vcc, v91, v55
	v_cmp_le_i32_e64 s[4:5], s8, v91
	s_and_b64 vcc, vcc, s[4:5]
	v_or_b32_e32 v92, 2, v91
	v_cndmask_b32_e32 v35, v85, v35, vcc
	v_cmp_gt_u32_e32 vcc, v92, v55
	v_cmp_lt_i32_e64 s[4:5], s8, v92
	s_and_b64 vcc, vcc, s[4:5]
	v_or_b32_e32 v91, 3, v91
	v_cndmask_b32_e32 v36, v85, v36, vcc
	v_cmp_gt_u32_e32 vcc, v91, v55
	v_cmp_lt_i32_e64 s[4:5], s8, v91
	s_and_b64 vcc, vcc, s[4:5]
	v_or_b32_e32 v91, v99, v66
	v_cndmask_b32_e32 v37, v85, v37, vcc
	v_cmp_gt_u32_e32 vcc, v91, v55
	v_cmp_lt_i32_e64 s[4:5], s8, v91
	s_and_b64 vcc, vcc, s[4:5]
	v_cndmask_b32_e32 v30, v85, v30, vcc
	v_cmp_ge_u32_e32 vcc, v91, v55
	v_cmp_le_i32_e64 s[4:5], s8, v91
	s_and_b64 vcc, vcc, s[4:5]
	v_or_b32_e32 v92, 2, v91
	v_cndmask_b32_e32 v31, v85, v31, vcc
	v_cmp_gt_u32_e32 vcc, v92, v55
	v_cmp_lt_i32_e64 s[4:5], s8, v92
	s_and_b64 vcc, vcc, s[4:5]
	v_or_b32_e32 v91, 3, v91
	v_cndmask_b32_e32 v32, v85, v32, vcc
	v_cmp_gt_u32_e32 vcc, v91, v55
	v_cmp_lt_i32_e64 s[4:5], s8, v91
	v_add_u32_e32 v90, 0x80, v55
	s_and_b64 vcc, vcc, s[4:5]
	v_or_b32_e32 v91, v100, v66
	v_cndmask_b32_e32 v33, v85, v33, vcc
	v_cmp_gt_u32_e32 vcc, v91, v55
	v_cmp_le_u32_e64 s[4:5], v91, v90
	s_and_b64 s[4:5], vcc, s[4:5]
	v_cmp_lt_i32_e32 vcc, s8, v91
	s_and_b64 vcc, s[4:5], vcc
	v_cmp_lt_u32_e64 s[4:5], v91, v90
	v_cndmask_b32_e32 v26, v85, v26, vcc
	v_cmp_ge_u32_e32 vcc, v91, v55
	s_and_b64 s[4:5], vcc, s[4:5]
	v_cmp_le_i32_e32 vcc, s8, v91
	s_and_b64 vcc, s[4:5], vcc
	v_or_b32_e32 v92, 2, v91
	v_cndmask_b32_e32 v27, v85, v27, vcc
	v_cmp_gt_u32_e32 vcc, v92, v55
	v_cmp_le_u32_e64 s[4:5], v92, v90
	s_and_b64 s[4:5], vcc, s[4:5]
	v_cmp_lt_i32_e32 vcc, s8, v92
	s_and_b64 vcc, s[4:5], vcc
	v_or_b32_e32 v91, 3, v91
	v_cndmask_b32_e32 v28, v85, v28, vcc
	v_cmp_gt_u32_e32 vcc, v91, v55
	v_cmp_le_u32_e64 s[4:5], v91, v90
	s_and_b64 s[4:5], vcc, s[4:5]
	v_cmp_lt_i32_e32 vcc, s8, v91
	s_and_b64 vcc, s[4:5], vcc
	v_or_b32_e32 v91, v101, v66
	v_cndmask_b32_e32 v29, v85, v29, vcc
	v_cmp_gt_u32_e32 vcc, v91, v55
	v_cmp_le_u32_e64 s[4:5], v91, v90
	s_and_b64 s[4:5], vcc, s[4:5]
	v_cmp_lt_i32_e32 vcc, s8, v91
	s_and_b64 vcc, s[4:5], vcc
	v_cmp_lt_u32_e64 s[4:5], v91, v90
	v_cndmask_b32_e32 v22, v85, v22, vcc
	v_cmp_ge_u32_e32 vcc, v91, v55
	s_and_b64 s[4:5], vcc, s[4:5]
	v_cmp_le_i32_e32 vcc, s8, v91
	s_and_b64 vcc, s[4:5], vcc
	v_or_b32_e32 v92, 2, v91
	v_cndmask_b32_e32 v23, v85, v23, vcc
	v_cmp_gt_u32_e32 vcc, v92, v55
	v_cmp_le_u32_e64 s[4:5], v92, v90
	s_and_b64 s[4:5], vcc, s[4:5]
	v_cmp_lt_i32_e32 vcc, s8, v92
	s_and_b64 vcc, s[4:5], vcc
	v_or_b32_e32 v91, 3, v91
	v_cndmask_b32_e32 v24, v85, v24, vcc
	v_cmp_gt_u32_e32 vcc, v91, v55
	v_cmp_le_u32_e64 s[4:5], v91, v90
	s_and_b64 s[4:5], vcc, s[4:5]
	v_cmp_lt_i32_e32 vcc, s8, v91
	s_and_b64 vcc, s[4:5], vcc
	v_or_b32_e32 v91, v102, v66
	v_cndmask_b32_e32 v25, v85, v25, vcc
	v_cmp_gt_u32_e32 vcc, v91, v55
	v_cmp_le_u32_e64 s[4:5], v91, v90
	s_and_b64 s[4:5], vcc, s[4:5]
	v_cmp_lt_i32_e32 vcc, s8, v91
	s_and_b64 vcc, s[4:5], vcc
	v_cmp_lt_u32_e64 s[4:5], v91, v90
	v_cndmask_b32_e32 v18, v85, v18, vcc
	v_cmp_ge_u32_e32 vcc, v91, v55
	s_and_b64 s[4:5], vcc, s[4:5]
	v_cmp_le_i32_e32 vcc, s8, v91
	s_and_b64 vcc, s[4:5], vcc
	v_or_b32_e32 v92, 2, v91
	v_cndmask_b32_e32 v19, v85, v19, vcc
	v_cmp_gt_u32_e32 vcc, v92, v55
	v_cmp_le_u32_e64 s[4:5], v92, v90
	s_and_b64 s[4:5], vcc, s[4:5]
	v_cmp_lt_i32_e32 vcc, s8, v92
	s_and_b64 vcc, s[4:5], vcc
	v_or_b32_e32 v91, 3, v91
	v_cndmask_b32_e32 v20, v85, v20, vcc
	v_cmp_gt_u32_e32 vcc, v91, v55
	v_cmp_le_u32_e64 s[4:5], v91, v90
	s_and_b64 s[4:5], vcc, s[4:5]
	v_cmp_lt_i32_e32 vcc, s8, v91
	s_and_b64 vcc, s[4:5], vcc
	v_or_b32_e32 v91, v103, v66
	v_cndmask_b32_e32 v21, v85, v21, vcc
	v_cmp_gt_u32_e32 vcc, v91, v55
	v_cmp_le_u32_e64 s[4:5], v91, v90
	s_and_b64 s[4:5], vcc, s[4:5]
	v_cmp_lt_i32_e32 vcc, s8, v91
	s_and_b64 vcc, s[4:5], vcc
	v_cmp_lt_u32_e64 s[4:5], v91, v90
	v_cndmask_b32_e32 v14, v85, v14, vcc
	v_cmp_ge_u32_e32 vcc, v91, v55
	s_and_b64 s[4:5], vcc, s[4:5]
	v_cmp_le_i32_e32 vcc, s8, v91
	s_and_b64 vcc, s[4:5], vcc
	v_or_b32_e32 v92, 2, v91
	v_cndmask_b32_e32 v15, v85, v15, vcc
	v_cmp_gt_u32_e32 vcc, v92, v55
	v_cmp_le_u32_e64 s[4:5], v92, v90
	s_and_b64 s[4:5], vcc, s[4:5]
	v_cmp_lt_i32_e32 vcc, s8, v92
	s_and_b64 vcc, s[4:5], vcc
	v_or_b32_e32 v91, 3, v91
	v_cndmask_b32_e32 v16, v85, v16, vcc
	v_cmp_gt_u32_e32 vcc, v91, v55
	v_cmp_le_u32_e64 s[4:5], v91, v90
	s_and_b64 s[4:5], vcc, s[4:5]
	v_cmp_lt_i32_e32 vcc, s8, v91
	s_and_b64 vcc, s[4:5], vcc
	v_or_b32_e32 v91, v104, v66
	v_cndmask_b32_e32 v17, v85, v17, vcc
	v_cmp_gt_u32_e32 vcc, v91, v55
	v_cmp_le_u32_e64 s[4:5], v91, v90
	s_and_b64 s[4:5], vcc, s[4:5]
	v_cmp_lt_i32_e32 vcc, s8, v91
	s_and_b64 vcc, s[4:5], vcc
	v_cmp_lt_u32_e64 s[4:5], v91, v90
	v_cndmask_b32_e32 v10, v85, v10, vcc
	v_cmp_ge_u32_e32 vcc, v91, v55
	v_max3_f32 v89, v89, v34, v35
	s_and_b64 s[4:5], vcc, s[4:5]
	v_cmp_le_i32_e32 vcc, s8, v91
	v_max3_f32 v89, v89, v36, v37
	s_and_b64 vcc, s[4:5], vcc
	v_or_b32_e32 v92, 2, v91
	v_max3_f32 v89, v89, v30, v31
	v_cndmask_b32_e32 v11, v85, v11, vcc
	v_cmp_gt_u32_e32 vcc, v92, v55
	v_cmp_le_u32_e64 s[4:5], v92, v90
	v_max3_f32 v89, v89, v32, v33
	s_and_b64 s[4:5], vcc, s[4:5]
	v_cmp_lt_i32_e32 vcc, s8, v92
	v_max3_f32 v89, v89, v26, v27
	s_and_b64 vcc, s[4:5], vcc
	v_or_b32_e32 v91, 3, v91
	v_max3_f32 v89, v89, v28, v29
	v_cndmask_b32_e32 v12, v85, v12, vcc
	v_cmp_gt_u32_e32 vcc, v91, v55
	v_cmp_le_u32_e64 s[4:5], v91, v90
	v_max3_f32 v89, v89, v22, v23
	s_and_b64 s[4:5], vcc, s[4:5]
	v_cmp_lt_i32_e32 vcc, s8, v91
	v_max3_f32 v89, v89, v24, v25
	s_and_b64 vcc, s[4:5], vcc
	v_or_b32_e32 v91, v105, v66
	v_max3_f32 v89, v89, v18, v19
	v_cndmask_b32_e32 v13, v85, v13, vcc
	v_cmp_le_u32_e32 vcc, v91, v90
	v_max3_f32 v89, v89, v20, v21
	v_or_b32_e32 v92, 2, v91
	v_cndmask_b32_e32 v6, v85, v6, vcc
	v_cmp_lt_u32_e32 vcc, v91, v90
	v_max3_f32 v89, v89, v14, v15
	v_or_b32_e32 v91, 3, v91
	v_cndmask_b32_e32 v7, v85, v7, vcc
	v_cmp_le_u32_e32 vcc, v92, v90
	v_max3_f32 v89, v89, v16, v17
	v_max3_f32 v89, v89, v10, v11
	v_cndmask_b32_e32 v8, v85, v8, vcc
	v_cmp_le_u32_e32 vcc, v91, v90
	v_or_b32_e32 v91, v106, v66
	v_max3_f32 v89, v89, v12, v13
	v_cndmask_b32_e32 v9, v85, v9, vcc
	v_cmp_le_u32_e32 vcc, v91, v90
	v_or_b32_e32 v92, 2, v91
	v_max3_f32 v89, v89, v6, v7
	v_cndmask_b32_e32 v2, v85, v2, vcc
	v_cmp_lt_u32_e32 vcc, v91, v90
	v_or_b32_e32 v91, 3, v91
	v_max3_f32 v89, v89, v8, v9
	v_cndmask_b32_e32 v3, v85, v3, vcc
	v_cmp_le_u32_e32 vcc, v92, v90
	v_max3_f32 v89, v89, v2, v3
	v_add_u32_e32 v55, 16, v55
	v_cndmask_b32_e32 v4, v85, v4, vcc
	v_cmp_le_u32_e32 vcc, v91, v90
	s_nop 1
	v_cndmask_b32_e32 v5, v85, v5, vcc
	v_max3_f32 v89, v89, v4, v5
	ds_bpermute_b32 v90, v67, v89
	s_waitcnt lgkmcnt(0)
	v_max_f32_e32 v90, v90, v90
	v_max_f32_e32 v89, v89, v90
	ds_bpermute_b32 v90, v68, v89
	s_waitcnt lgkmcnt(0)
	v_max3_f32 v89, v89, v90, v53
	v_sub_f32_e32 v38, v38, v89
	v_mul_f32_e32 v38, 0x3fb8aa3b, v38
	v_sub_f32_e32 v39, v39, v89
	v_exp_f32_e32 v38, v38
	v_mul_f32_e32 v39, 0x3fb8aa3b, v39
	v_sub_f32_e32 v40, v40, v89
	v_exp_f32_e32 v39, v39
	v_mul_f32_e32 v40, 0x3fb8aa3b, v40
	v_sub_f32_e32 v41, v41, v89
	v_exp_f32_e32 v40, v40
	v_mul_f32_e32 v41, 0x3fb8aa3b, v41
	v_sub_f32_e32 v34, v34, v89
	v_exp_f32_e32 v41, v41
	v_mul_f32_e32 v34, 0x3fb8aa3b, v34
	v_sub_f32_e32 v35, v35, v89
	v_add_f32_e32 v90, 0, v38
	v_exp_f32_e32 v34, v34
	v_mul_f32_e32 v35, 0x3fb8aa3b, v35
	v_sub_f32_e32 v36, v36, v89
	v_add_f32_e32 v90, v39, v90
	v_exp_f32_e32 v35, v35
	v_mul_f32_e32 v36, 0x3fb8aa3b, v36
	v_sub_f32_e32 v37, v37, v89
	v_add_f32_e32 v90, v40, v90
	v_exp_f32_e32 v36, v36
	v_mul_f32_e32 v37, 0x3fb8aa3b, v37
	v_sub_f32_e32 v30, v30, v89
	v_add_f32_e32 v90, v41, v90
	v_exp_f32_e32 v37, v37
	v_mul_f32_e32 v30, 0x3fb8aa3b, v30
	v_sub_f32_e32 v31, v31, v89
	v_add_f32_e32 v90, v34, v90
	v_exp_f32_e32 v30, v30
	v_mul_f32_e32 v31, 0x3fb8aa3b, v31
	v_sub_f32_e32 v32, v32, v89
	v_add_f32_e32 v90, v35, v90
	v_exp_f32_e32 v31, v31
	v_mul_f32_e32 v32, 0x3fb8aa3b, v32
	v_sub_f32_e32 v33, v33, v89
	v_add_f32_e32 v90, v36, v90
	v_exp_f32_e32 v32, v32
	v_mul_f32_e32 v33, 0x3fb8aa3b, v33
	v_sub_f32_e32 v26, v26, v89
	v_add_f32_e32 v90, v37, v90
	v_exp_f32_e32 v33, v33
	v_mul_f32_e32 v26, 0x3fb8aa3b, v26
	v_sub_f32_e32 v27, v27, v89
	v_add_f32_e32 v90, v30, v90
	v_exp_f32_e32 v26, v26
	v_mul_f32_e32 v27, 0x3fb8aa3b, v27
	v_sub_f32_e32 v28, v28, v89
	v_add_f32_e32 v90, v31, v90
	v_exp_f32_e32 v27, v27
	v_mul_f32_e32 v28, 0x3fb8aa3b, v28
	v_sub_f32_e32 v29, v29, v89
	v_add_f32_e32 v90, v32, v90
	v_exp_f32_e32 v28, v28
	v_mul_f32_e32 v29, 0x3fb8aa3b, v29
	v_sub_f32_e32 v22, v22, v89
	v_add_f32_e32 v90, v33, v90
	v_exp_f32_e32 v29, v29
	v_mul_f32_e32 v22, 0x3fb8aa3b, v22
	v_add_f32_e32 v90, v26, v90
	v_exp_f32_e32 v91, v22
	v_add_f32_e32 v90, v27, v90
	v_add_f32_e32 v90, v28, v90
	v_sub_f32_e32 v23, v23, v89
	v_add_f32_e32 v90, v29, v90
	v_mul_f32_e32 v23, 0x3fb8aa3b, v23
	v_add_f32_e32 v22, v91, v90
	v_exp_f32_e32 v90, v23
	v_sub_f32_e32 v23, v24, v89
	v_mul_f32_e32 v23, 0x3fb8aa3b, v23
	v_exp_f32_e32 v92, v23
	v_sub_f32_e32 v23, v25, v89
	v_sub_f32_e32 v19, v19, v89
	v_mul_f32_e32 v23, 0x3fb8aa3b, v23
	v_sub_f32_e32 v18, v18, v89
	v_mul_f32_e32 v19, 0x3fb8aa3b, v19
	v_exp_f32_e32 v93, v23
	v_mul_f32_e32 v18, 0x3fb8aa3b, v18
	v_exp_f32_e32 v95, v19
	v_sub_f32_e32 v19, v20, v89
	v_exp_f32_e32 v94, v18
	v_mul_f32_e32 v19, 0x3fb8aa3b, v19
	v_add_f32_e32 v22, v90, v22
	v_exp_f32_e32 v96, v19
	v_sub_f32_e32 v19, v21, v89
	v_sub_f32_e32 v15, v15, v89
	v_add_f32_e32 v22, v92, v22
	v_mul_f32_e32 v19, 0x3fb8aa3b, v19
	v_sub_f32_e32 v14, v14, v89
	v_mul_f32_e32 v15, 0x3fb8aa3b, v15
	v_add_f32_e32 v22, v93, v22
	v_exp_f32_e32 v97, v19
	v_mul_f32_e32 v14, 0x3fb8aa3b, v14
	v_exp_f32_e32 v99, v15
	v_sub_f32_e32 v15, v16, v89
	v_add_f32_e32 v18, v94, v22
	v_exp_f32_e32 v98, v14
	v_mul_f32_e32 v15, 0x3fb8aa3b, v15
	v_add_f32_e32 v18, v95, v18
	v_exp_f32_e32 v100, v15
	v_sub_f32_e32 v15, v17, v89
	v_sub_f32_e32 v11, v11, v89
	v_add_f32_e32 v18, v96, v18
	v_mul_f32_e32 v15, 0x3fb8aa3b, v15
	v_sub_f32_e32 v10, v10, v89
	v_mul_f32_e32 v11, 0x3fb8aa3b, v11
	v_add_f32_e32 v18, v97, v18
	v_exp_f32_e32 v101, v15
	v_mul_f32_e32 v10, 0x3fb8aa3b, v10
	v_exp_f32_e32 v103, v11
	v_sub_f32_e32 v11, v12, v89
	v_add_f32_e32 v14, v98, v18
	v_exp_f32_e32 v102, v10
	v_mul_f32_e32 v11, 0x3fb8aa3b, v11
	v_add_f32_e32 v14, v99, v14
	v_exp_f32_e32 v104, v11
	v_sub_f32_e32 v11, v13, v89
	v_sub_f32_e32 v7, v7, v89
	v_add_f32_e32 v14, v100, v14
	v_mul_f32_e32 v11, 0x3fb8aa3b, v11
	v_sub_f32_e32 v6, v6, v89
	v_mul_f32_e32 v7, 0x3fb8aa3b, v7
	v_add_f32_e32 v14, v101, v14
	v_exp_f32_e32 v105, v11
	v_mul_f32_e32 v6, 0x3fb8aa3b, v6
	v_exp_f32_e32 v107, v7
	v_sub_f32_e32 v7, v8, v89
	v_add_f32_e32 v10, v102, v14
	v_exp_f32_e32 v106, v6
	v_mul_f32_e32 v7, 0x3fb8aa3b, v7
	v_add_f32_e32 v10, v103, v10
	v_exp_f32_e32 v108, v7
	v_sub_f32_e32 v7, v9, v89
	v_sub_f32_e32 v3, v3, v89
	v_add_f32_e32 v10, v104, v10
	v_mul_f32_e32 v7, 0x3fb8aa3b, v7
	v_sub_f32_e32 v2, v2, v89
	v_mul_f32_e32 v3, 0x3fb8aa3b, v3
	v_add_f32_e32 v10, v105, v10
	v_exp_f32_e32 v109, v7
	v_mul_f32_e32 v2, 0x3fb8aa3b, v2
	v_exp_f32_e32 v111, v3
	v_sub_f32_e32 v3, v4, v89
	v_add_f32_e32 v6, v106, v10
	v_exp_f32_e32 v110, v2
	v_mul_f32_e32 v3, 0x3fb8aa3b, v3
	v_add_f32_e32 v6, v107, v6
	v_exp_f32_e32 v112, v3
	v_sub_f32_e32 v3, v5, v89
	v_add_f32_e32 v6, v108, v6
	v_mul_f32_e32 v3, 0x3fb8aa3b, v3
	v_add_f32_e32 v6, v109, v6
	v_exp_f32_e32 v113, v3
	v_add_f32_e32 v2, v110, v6
	v_add_f32_e32 v2, v111, v2
	v_add_f32_e32 v2, v112, v2
	v_add_f32_e32 v2, v113, v2
	ds_bpermute_b32 v3, v67, v2
	v_lshl_add_u32 v18, v88, 5, v73
	v_add_u32_e32 v10, 0xb000, v18
	v_add_u32_e32 v14, 0xd000, v18
	s_waitcnt lgkmcnt(0)
	v_add_f32_e32 v2, v2, v3
	ds_bpermute_b32 v3, v68, v2
	s_waitcnt lgkmcnt(0)
	v_add_f32_e32 v2, v2, v3
	v_sub_f32_e32 v3, v53, v89
	v_mul_f32_e32 v3, 0x3fb8aa3b, v3
	v_exp_f32_e32 v3, v3
	s_nop 0
	v_add_f32_e32 v2, v3, v2
	v_div_scale_f32 v3, s[4:5], v2, v2, 1.0
	v_rcp_f32_e32 v4, v3
	s_nop 0
	v_fma_f32 v5, -v3, v4, 1.0
	v_fmac_f32_e32 v4, v5, v4
	v_div_scale_f32 v5, vcc, 1.0, v2, 1.0
	v_mul_f32_e32 v6, v5, v4
	v_fma_f32 v7, -v3, v6, v5
	v_fmac_f32_e32 v6, v7, v4
	v_fma_f32 v3, -v3, v6, v5
	v_div_fmas_f32 v3, v3, v4, v6
	v_div_fixup_f32 v89, v3, v2, 1.0
	v_mul_f32_e32 v2, v38, v89
	v_mul_f32_e32 v3, v39, v89
	v_cvt_pk_bf16_f32 v2, v2, v3
	v_mul_f32_e32 v3, v40, v89
	v_mul_f32_e32 v4, v41, v89
	v_cvt_pk_bf16_f32 v3, v3, v4
	v_mul_f32_e32 v4, v34, v89
	v_mul_f32_e32 v5, v35, v89
	v_cvt_pk_bf16_f32 v4, v4, v5
	v_mul_f32_e32 v5, v36, v89
	v_mul_f32_e32 v6, v37, v89
	v_cvt_pk_bf16_f32 v5, v5, v6
	v_add_u32_e32 v6, 0x9000, v18
	v_add_u32_e32 v18, 0xf000, v18
	ds_read2_b64 v[6:9], v6 offset1:4
	ds_read2_b64 v[10:13], v10 offset0:32 offset1:36
	ds_read2_b64 v[14:17], v14 offset0:64 offset1:68
	ds_read2_b64 v[18:21], v18 offset0:96 offset1:100
	s_waitcnt lgkmcnt(3)
	v_mfma_f32_16x16x32_bf16 v[6:9], v[6:9], v[2:5], 0
	v_mul_f32_e32 v22, v29, v89
	s_waitcnt lgkmcnt(2)
	v_mfma_f32_16x16x32_bf16 v[10:13], v[10:13], v[2:5], 0
	s_waitcnt lgkmcnt(1)
	v_mfma_f32_16x16x32_bf16 v[14:17], v[14:17], v[2:5], 0
	s_waitcnt lgkmcnt(0)
	v_mfma_f32_16x16x32_bf16 v[2:5], v[18:21], v[2:5], 0
	v_mul_f32_e32 v18, v30, v89
	v_mul_f32_e32 v19, v31, v89
	v_cvt_pk_bf16_f32 v18, v18, v19
	v_mul_f32_e32 v19, v32, v89
	v_mul_f32_e32 v20, v33, v89
	v_cvt_pk_bf16_f32 v19, v19, v20
	v_mul_f32_e32 v20, v26, v89
	v_mul_f32_e32 v21, v27, v89
	v_cvt_pk_bf16_f32 v20, v20, v21
	v_mul_f32_e32 v21, v28, v89
	v_lshl_add_u32 v26, v87, 5, v73
	v_cvt_pk_bf16_f32 v21, v21, v22
	v_add_u32_e32 v22, 0x9000, v26
	ds_read2_b64 v[22:25], v22 offset1:4
	s_waitcnt lgkmcnt(0)
	v_mfma_f32_16x16x32_bf16 v[6:9], v[22:25], v[18:21], v[6:9]
	v_add_u32_e32 v22, 0xb000, v26
	ds_read2_b64 v[22:25], v22 offset0:32 offset1:36
	s_waitcnt lgkmcnt(0)
	v_mfma_f32_16x16x32_bf16 v[10:13], v[22:25], v[18:21], v[10:13]
	v_add_u32_e32 v22, 0xd000, v26
	ds_read2_b64 v[22:25], v22 offset0:64 offset1:68
	s_waitcnt lgkmcnt(0)
	v_mfma_f32_16x16x32_bf16 v[14:17], v[22:25], v[18:21], v[14:17]
	v_add_u32_e32 v22, 0xf000, v26
	ds_read2_b64 v[22:25], v22 offset0:96 offset1:100
	v_lshl_add_u32 v26, v86, 5, v73
	s_waitcnt lgkmcnt(0)
	v_mfma_f32_16x16x32_bf16 v[2:5], v[22:25], v[18:21], v[2:5]
	v_mul_f32_e32 v18, v91, v89
	v_mul_f32_e32 v19, v90, v89
	v_cvt_pk_bf16_f32 v18, v18, v19
	v_mul_f32_e32 v19, v92, v89
	v_mul_f32_e32 v20, v93, v89
	v_cvt_pk_bf16_f32 v19, v19, v20
	v_mul_f32_e32 v20, v94, v89
	v_mul_f32_e32 v21, v95, v89
	v_cvt_pk_bf16_f32 v20, v20, v21
	v_mul_f32_e32 v21, v96, v89
	v_mul_f32_e32 v22, v97, v89
	v_cvt_pk_bf16_f32 v21, v21, v22
	v_add_u32_e32 v22, 0x9000, v26
	ds_read2_b64 v[22:25], v22 offset1:4
	s_waitcnt lgkmcnt(0)
	v_mfma_f32_16x16x32_bf16 v[6:9], v[22:25], v[18:21], v[6:9]
	v_add_u32_e32 v22, 0xb000, v26
	ds_read2_b64 v[22:25], v22 offset0:32 offset1:36
	s_waitcnt lgkmcnt(0)
	v_mfma_f32_16x16x32_bf16 v[10:13], v[22:25], v[18:21], v[10:13]
	v_add_u32_e32 v22, 0xd000, v26
	ds_read2_b64 v[22:25], v22 offset0:64 offset1:68
	s_waitcnt lgkmcnt(0)
	v_mfma_f32_16x16x32_bf16 v[14:17], v[22:25], v[18:21], v[14:17]
	v_add_u32_e32 v22, 0xf000, v26
	ds_read2_b64 v[22:25], v22 offset0:96 offset1:100
	v_lshl_add_u32 v26, v59, 5, v73
	s_waitcnt lgkmcnt(0)
	v_mfma_f32_16x16x32_bf16 v[2:5], v[22:25], v[18:21], v[2:5]
	v_mul_f32_e32 v18, v98, v89
	v_mul_f32_e32 v19, v99, v89
	v_cvt_pk_bf16_f32 v18, v18, v19
	v_mul_f32_e32 v19, v100, v89
	v_mul_f32_e32 v20, v101, v89
	v_cvt_pk_bf16_f32 v19, v19, v20
	v_mul_f32_e32 v20, v102, v89
	v_mul_f32_e32 v21, v103, v89
	v_cvt_pk_bf16_f32 v20, v20, v21
	v_mul_f32_e32 v21, v104, v89
	v_mul_f32_e32 v22, v105, v89
	v_cvt_pk_bf16_f32 v21, v21, v22
	v_add_u32_e32 v22, 0x9000, v26
	ds_read2_b64 v[22:25], v22 offset1:4
	s_waitcnt lgkmcnt(0)
	v_mfma_f32_16x16x32_bf16 v[6:9], v[22:25], v[18:21], v[6:9]
	v_add_u32_e32 v22, 0xb000, v26
	ds_read2_b64 v[22:25], v22 offset0:32 offset1:36
	s_waitcnt lgkmcnt(0)
	v_mfma_f32_16x16x32_bf16 v[10:13], v[22:25], v[18:21], v[10:13]
	v_add_u32_e32 v22, 0xd000, v26
	ds_read2_b64 v[22:25], v22 offset0:64 offset1:68
	s_waitcnt lgkmcnt(0)
	v_mfma_f32_16x16x32_bf16 v[14:17], v[22:25], v[18:21], v[14:17]
	v_add_u32_e32 v22, 0xf000, v26
	ds_read2_b64 v[22:25], v22 offset0:96 offset1:100
	v_lshl_add_u32 v26, v57, 5, v73
	s_waitcnt lgkmcnt(0)
	v_mfma_f32_16x16x32_bf16 v[18:21], v[22:25], v[18:21], v[2:5]
	s_nop 2
	v_mul_f32_e32 v2, v106, v89
	v_mul_f32_e32 v3, v107, v89
	v_cvt_pk_bf16_f32 v22, v2, v3
	v_mul_f32_e32 v2, v108, v89
	v_mul_f32_e32 v3, v109, v89
	v_cvt_pk_bf16_f32 v23, v2, v3
	v_mul_f32_e32 v2, v110, v89
	v_mul_f32_e32 v3, v111, v89
	v_cvt_pk_bf16_f32 v24, v2, v3
	v_mul_f32_e32 v2, v112, v89
	v_mul_f32_e32 v3, v113, v89
	v_cvt_pk_bf16_f32 v25, v2, v3
	v_add_u32_e32 v2, 0x9000, v26
	ds_read2_b64 v[2:5], v2 offset1:4
	s_waitcnt lgkmcnt(0)
	v_mfma_f32_16x16x32_bf16 v[2:5], v[2:5], v[22:25], v[6:9]
	s_nop 2
	v_add_u32_e32 v6, 0xb000, v26
	ds_read2_b64 v[6:9], v6 offset0:32 offset1:36
	s_nop 2
	v_cvt_pk_bf16_f32 v2, v2, v3
	s_waitcnt lgkmcnt(0)
	v_mfma_f32_16x16x32_bf16 v[6:9], v[6:9], v[22:25], v[10:13]
	s_nop 2
	v_add_u32_e32 v10, 0xd000, v26
	ds_read2_b64 v[10:13], v10 offset0:64 offset1:68
	v_cvt_pk_bf16_f32 v3, v4, v5
	s_waitcnt lgkmcnt(0)
	v_mfma_f32_16x16x32_bf16 v[10:13], v[10:13], v[22:25], v[14:17]
	s_nop 2
	v_add_u32_e32 v14, 0xf000, v26
	ds_read2_b64 v[14:17], v14 offset0:96 offset1:100
	s_waitcnt lgkmcnt(0)
	v_mfma_f32_16x16x32_bf16 v[14:17], v[14:17], v[22:25], v[18:21]
	s_nop 2
	v_lshl_add_u64 v[18:19], v[62:63], 0, s[10:11]
	global_store_dwordx2 v[18:19], v[2:3], off offset:-64
	v_cvt_pk_bf16_f32 v2, v6, v7
	v_cvt_pk_bf16_f32 v3, v8, v9
	s_add_u32 s10, s10, 0x8000
	global_store_dwordx2 v[18:19], v[2:3], off offset:-32
	v_cvt_pk_bf16_f32 v2, v10, v11
	v_cvt_pk_bf16_f32 v3, v12, v13
	s_addc_u32 s11, s11, 0
	global_store_dwordx2 v[18:19], v[2:3], off
	v_cvt_pk_bf16_f32 v2, v14, v15
	v_cvt_pk_bf16_f32 v3, v16, v17
	s_cmp_eq_u32 s10, 0x20000
	global_store_dwordx2 v[18:19], v[2:3], off offset:32
	s_cbranch_scc0 .LBB0_559
	s_add_i32 s14, s14, s3
	s_add_i32 s18, s18, s19
	s_cmpk_gt_i32 s14, 0x1ff
	s_cbranch_scc0 .LBB0_549
